# MoE1 SwiGLU epilogue issued as packed f32 pairs (same ops, same order per value), in place on accumulators
# speedup vs baseline: 1.0026x; 1.0001x over previous
.LBB0_1284:
	v_mov_b32_e32 v2, v0
	s_nop 15
	s_nop 15
	s_bitcmp1_b32 s33, 0
	v_readfirstlane_b32 s4, v2
	s_cselect_b32 s5, 0xc00, 0
	s_ashr_i32 s23, s4, 2
	s_andn2_b32 s23, s23, 63
	v_and_b32_e32 v3, 15, v2
	s_add_i32 s23, s23, s95
	s_lshr_b32 s4, s4, 1
	v_add_u32_e32 v18, s23, v3
	s_lshl_b32 s23, s26, 7
	s_and_b32 s4, s4, 0x60
	s_add_i32 s5, s80, s5
	s_or_b32 s23, s4, s23
	v_lshrrev_b32_e32 v2, 1, v2
	s_lshl_b32 s4, s4, 2
	v_and_b32_e32 v2, 24, v2
	s_add_i32 s5, s5, s4
	v_lshl_add_u32 v6, v2, 2, s5
	v_or_b32_e32 v20, s23, v2
	ds_read_b128 v[10:13], v6
	ds_read_b128 v[2:5], v6 offset:16
	ds_read_b128 v[14:17], v6 offset:512
	ds_read_b128 v[6:9], v6 offset:528
	v_ashrrev_i32_e32 v21, 31, v20
	s_waitcnt lgkmcnt(0)
	v_ashrrev_i32_e32 v19, 31, v18
	v_mov_b32_e32 v210, 0x3d000000
	v_mov_b32_e32 v211, 0x3d000000
	v_lshlrev_b64 v[18:19], 10, v[18:19]
	v_mov_b32_e32 v212, 0x3fd9db23
	v_mov_b32_e32 v213, 0x3fd9db23
	v_lshl_add_u64 v[18:19], s[12:13], 0, v[18:19]
	v_mov_b32_e32 v214, 0xbfb8aa3b
	v_mov_b32_e32 v215, 0xbfb8aa3b
	v_lshl_add_u64 v[18:19], v[18:19], 0, v[20:21]
	v_mov_b32_e32 v216, 1.0
	v_mov_b32_e32 v217, 1.0
	v_pk_fma_f32 v[154:155], v[154:155], v[210:211], v[10:11]
	v_pk_fma_f32 v[156:157], v[156:157], v[210:211], v[12:13]
	v_pk_fma_f32 v[146:147], v[146:147], v[210:211], v[2:3]
	v_pk_fma_f32 v[148:149], v[148:149], v[210:211], v[4:5]
	v_min_f32_e32 v154, 0x40e00000, v154
	v_min_f32_e32 v155, 0x40e00000, v155
	v_min_f32_e32 v156, 0x40e00000, v156
	v_min_f32_e32 v157, 0x40e00000, v157
	v_min_f32_e32 v146, 0x40e00000, v146
	v_min_f32_e32 v147, 0x40e00000, v147
	v_min_f32_e32 v148, 0x40e00000, v148
	v_min_f32_e32 v149, 0x40e00000, v149
	v_pk_mul_f32 v[202:203], v[154:155], v[212:213]
	v_pk_mul_f32 v[204:205], v[156:157], v[212:213]
	v_pk_mul_f32 v[206:207], v[146:147], v[212:213]
	v_pk_mul_f32 v[208:209], v[148:149], v[212:213]
	v_pk_fma_f32 v[158:159], v[158:159], v[210:211], v[14:15]
	v_pk_fma_f32 v[160:161], v[160:161], v[210:211], v[16:17]
	v_pk_fma_f32 v[150:151], v[150:151], v[210:211], v[6:7]
	v_pk_fma_f32 v[152:153], v[152:153], v[210:211], v[8:9]
	v_pk_mul_f32 v[202:203], v[202:203], v[214:215]
	v_pk_mul_f32 v[204:205], v[204:205], v[214:215]
	v_pk_mul_f32 v[206:207], v[206:207], v[214:215]
	v_pk_mul_f32 v[208:209], v[208:209], v[214:215]
	v_med3_f32 v158, v158, s37, v243
	v_med3_f32 v159, v159, s37, v243
	v_med3_f32 v160, v160, s37, v243
	v_med3_f32 v161, v161, s37, v243
	v_med3_f32 v150, v150, s37, v243
	v_med3_f32 v151, v151, s37, v243
	v_med3_f32 v152, v152, s37, v243
	v_med3_f32 v153, v153, s37, v243
	v_exp_f32_e32 v202, v202
	v_exp_f32_e32 v203, v203
	v_exp_f32_e32 v204, v204
	v_exp_f32_e32 v205, v205
	v_exp_f32_e32 v206, v206
	v_exp_f32_e32 v207, v207
	v_exp_f32_e32 v208, v208
	v_exp_f32_e32 v209, v209
	v_pk_add_f32 v[158:159], v[158:159], v[216:217]
	v_pk_add_f32 v[160:161], v[160:161], v[216:217]
	v_pk_add_f32 v[150:151], v[150:151], v[216:217]
	v_pk_add_f32 v[152:153], v[152:153], v[216:217]
	v_pk_add_f32 v[202:203], v[202:203], v[216:217]
	v_pk_add_f32 v[204:205], v[204:205], v[216:217]
	v_pk_add_f32 v[206:207], v[206:207], v[216:217]
	v_pk_add_f32 v[208:209], v[208:209], v[216:217]
	v_rcp_f32_e32 v202, v202
	v_rcp_f32_e32 v203, v203
	v_rcp_f32_e32 v204, v204
	v_rcp_f32_e32 v205, v205
	v_rcp_f32_e32 v206, v206
	v_rcp_f32_e32 v207, v207
	v_rcp_f32_e32 v208, v208
	v_rcp_f32_e32 v209, v209
	v_pk_mul_f32 v[154:155], v[154:155], v[202:203]
	v_pk_mul_f32 v[156:157], v[156:157], v[204:205]
	v_pk_mul_f32 v[146:147], v[146:147], v[206:207]
	v_pk_mul_f32 v[148:149], v[148:149], v[208:209]
	v_pk_mul_f32 v[154:155], v[158:159], v[154:155]
	v_pk_mul_f32 v[156:157], v[160:161], v[156:157]
	v_pk_mul_f32 v[146:147], v[150:151], v[146:147]
	v_pk_mul_f32 v[148:149], v[152:153], v[148:149]
	v_cvt_pk_fp8_f32 v200, v154, v155
	v_cvt_pk_fp8_f32 v201, v146, v147
	v_cvt_pk_fp8_f32 v200, v156, v157 op_sel:[0,0,1]
	v_cvt_pk_fp8_f32 v201, v148, v149 op_sel:[0,0,1]
	global_store_dwordx2 v[18:19], v[200:201], off
	v_pk_fma_f32 v[138:139], v[138:139], v[210:211], v[10:11]
	v_pk_fma_f32 v[140:141], v[140:141], v[210:211], v[12:13]
	v_pk_fma_f32 v[130:131], v[130:131], v[210:211], v[2:3]
	v_pk_fma_f32 v[132:133], v[132:133], v[210:211], v[4:5]
	v_min_f32_e32 v138, 0x40e00000, v138
	v_min_f32_e32 v139, 0x40e00000, v139
	v_min_f32_e32 v140, 0x40e00000, v140
	v_min_f32_e32 v141, 0x40e00000, v141
	v_min_f32_e32 v130, 0x40e00000, v130
	v_min_f32_e32 v131, 0x40e00000, v131
	v_min_f32_e32 v132, 0x40e00000, v132
	v_min_f32_e32 v133, 0x40e00000, v133
	v_pk_mul_f32 v[202:203], v[138:139], v[212:213]
	v_pk_mul_f32 v[204:205], v[140:141], v[212:213]
	v_pk_mul_f32 v[206:207], v[130:131], v[212:213]
	v_pk_mul_f32 v[208:209], v[132:133], v[212:213]
	v_pk_fma_f32 v[142:143], v[142:143], v[210:211], v[14:15]
	v_pk_fma_f32 v[144:145], v[144:145], v[210:211], v[16:17]
	v_pk_fma_f32 v[134:135], v[134:135], v[210:211], v[6:7]
	v_pk_fma_f32 v[136:137], v[136:137], v[210:211], v[8:9]
	v_pk_mul_f32 v[202:203], v[202:203], v[214:215]
	v_pk_mul_f32 v[204:205], v[204:205], v[214:215]
	v_pk_mul_f32 v[206:207], v[206:207], v[214:215]
	v_pk_mul_f32 v[208:209], v[208:209], v[214:215]
	v_med3_f32 v142, v142, s37, v243
	v_med3_f32 v143, v143, s37, v243
	v_med3_f32 v144, v144, s37, v243
	v_med3_f32 v145, v145, s37, v243
	v_med3_f32 v134, v134, s37, v243
	v_med3_f32 v135, v135, s37, v243
	v_med3_f32 v136, v136, s37, v243
	v_med3_f32 v137, v137, s37, v243
	v_exp_f32_e32 v202, v202
	v_exp_f32_e32 v203, v203
	v_exp_f32_e32 v204, v204
	v_exp_f32_e32 v205, v205
	v_exp_f32_e32 v206, v206
	v_exp_f32_e32 v207, v207
	v_exp_f32_e32 v208, v208
	v_exp_f32_e32 v209, v209
	v_pk_add_f32 v[142:143], v[142:143], v[216:217]
	v_pk_add_f32 v[144:145], v[144:145], v[216:217]
	v_pk_add_f32 v[134:135], v[134:135], v[216:217]
	v_pk_add_f32 v[136:137], v[136:137], v[216:217]
	v_add_co_u32_e32 v194, vcc, 0x4000, v18
	v_pk_add_f32 v[202:203], v[202:203], v[216:217]
	v_pk_add_f32 v[204:205], v[204:205], v[216:217]
	v_pk_add_f32 v[206:207], v[206:207], v[216:217]
	v_pk_add_f32 v[208:209], v[208:209], v[216:217]
	v_addc_co_u32_e32 v195, vcc, 0, v19, vcc
	v_rcp_f32_e32 v202, v202
	v_rcp_f32_e32 v203, v203
	v_rcp_f32_e32 v204, v204
	v_rcp_f32_e32 v205, v205
	v_rcp_f32_e32 v206, v206
	v_rcp_f32_e32 v207, v207
	v_rcp_f32_e32 v208, v208
	v_rcp_f32_e32 v209, v209
	v_pk_mul_f32 v[138:139], v[138:139], v[202:203]
	v_pk_mul_f32 v[140:141], v[140:141], v[204:205]
	v_pk_mul_f32 v[130:131], v[130:131], v[206:207]
	v_pk_mul_f32 v[132:133], v[132:133], v[208:209]
	v_pk_mul_f32 v[138:139], v[142:143], v[138:139]
	v_pk_mul_f32 v[140:141], v[144:145], v[140:141]
	v_pk_mul_f32 v[130:131], v[134:135], v[130:131]
	v_pk_mul_f32 v[132:133], v[136:137], v[132:133]
	v_cvt_pk_fp8_f32 v196, v138, v139
	v_cvt_pk_fp8_f32 v197, v130, v131
	v_cvt_pk_fp8_f32 v196, v140, v141 op_sel:[0,0,1]
	v_cvt_pk_fp8_f32 v197, v132, v133 op_sel:[0,0,1]
	global_store_dwordx2 v[194:195], v[196:197], off
	v_pk_fma_f32 v[122:123], v[122:123], v[210:211], v[10:11]
	v_pk_fma_f32 v[124:125], v[124:125], v[210:211], v[12:13]
	v_pk_fma_f32 v[114:115], v[114:115], v[210:211], v[2:3]
	v_pk_fma_f32 v[116:117], v[116:117], v[210:211], v[4:5]
	v_min_f32_e32 v122, 0x40e00000, v122
	v_min_f32_e32 v123, 0x40e00000, v123
	v_min_f32_e32 v124, 0x40e00000, v124
	v_min_f32_e32 v125, 0x40e00000, v125
	v_min_f32_e32 v114, 0x40e00000, v114
	v_min_f32_e32 v115, 0x40e00000, v115
	v_min_f32_e32 v116, 0x40e00000, v116
	v_min_f32_e32 v117, 0x40e00000, v117
	v_pk_mul_f32 v[202:203], v[122:123], v[212:213]
	v_pk_mul_f32 v[204:205], v[124:125], v[212:213]
	v_pk_mul_f32 v[206:207], v[114:115], v[212:213]
	v_pk_mul_f32 v[208:209], v[116:117], v[212:213]
	v_pk_fma_f32 v[126:127], v[126:127], v[210:211], v[14:15]
	v_pk_fma_f32 v[128:129], v[128:129], v[210:211], v[16:17]
	v_pk_fma_f32 v[118:119], v[118:119], v[210:211], v[6:7]
	v_pk_fma_f32 v[120:121], v[120:121], v[210:211], v[8:9]
	v_pk_mul_f32 v[202:203], v[202:203], v[214:215]
	v_pk_mul_f32 v[204:205], v[204:205], v[214:215]
	v_pk_mul_f32 v[206:207], v[206:207], v[214:215]
	v_pk_mul_f32 v[208:209], v[208:209], v[214:215]
	v_med3_f32 v126, v126, s37, v243
	v_med3_f32 v127, v127, s37, v243
	v_med3_f32 v128, v128, s37, v243
	v_med3_f32 v129, v129, s37, v243
	v_med3_f32 v118, v118, s37, v243
	v_med3_f32 v119, v119, s37, v243
	v_med3_f32 v120, v120, s37, v243
	v_med3_f32 v121, v121, s37, v243
	v_exp_f32_e32 v202, v202
	v_exp_f32_e32 v203, v203
	v_exp_f32_e32 v204, v204
	v_exp_f32_e32 v205, v205
	v_exp_f32_e32 v206, v206
	v_exp_f32_e32 v207, v207
	v_exp_f32_e32 v208, v208
	v_exp_f32_e32 v209, v209
	v_pk_add_f32 v[126:127], v[126:127], v[216:217]
	v_pk_add_f32 v[128:129], v[128:129], v[216:217]
	v_pk_add_f32 v[118:119], v[118:119], v[216:217]
	v_pk_add_f32 v[120:121], v[120:121], v[216:217]
	v_add_co_u32_e32 v198, vcc, 0x8000, v18
	v_pk_add_f32 v[202:203], v[202:203], v[216:217]
	v_pk_add_f32 v[204:205], v[204:205], v[216:217]
	v_pk_add_f32 v[206:207], v[206:207], v[216:217]
	v_pk_add_f32 v[208:209], v[208:209], v[216:217]
	v_addc_co_u32_e32 v199, vcc, 0, v19, vcc
	v_rcp_f32_e32 v202, v202
	v_rcp_f32_e32 v203, v203
	v_rcp_f32_e32 v204, v204
	v_rcp_f32_e32 v205, v205
	v_rcp_f32_e32 v206, v206
	v_rcp_f32_e32 v207, v207
	v_rcp_f32_e32 v208, v208
	v_rcp_f32_e32 v209, v209
	v_pk_mul_f32 v[122:123], v[122:123], v[202:203]
	v_pk_mul_f32 v[124:125], v[124:125], v[204:205]
	v_pk_mul_f32 v[114:115], v[114:115], v[206:207]
	v_pk_mul_f32 v[116:117], v[116:117], v[208:209]
	v_pk_mul_f32 v[122:123], v[126:127], v[122:123]
	v_pk_mul_f32 v[124:125], v[128:129], v[124:125]
	v_pk_mul_f32 v[114:115], v[118:119], v[114:115]
	v_pk_mul_f32 v[116:117], v[120:121], v[116:117]
	v_cvt_pk_fp8_f32 v200, v122, v123
	v_cvt_pk_fp8_f32 v201, v114, v115
	v_cvt_pk_fp8_f32 v200, v124, v125 op_sel:[0,0,1]
	v_cvt_pk_fp8_f32 v201, v116, v117 op_sel:[0,0,1]
	global_store_dwordx2 v[198:199], v[200:201], off
	v_pk_fma_f32 v[106:107], v[106:107], v[210:211], v[10:11]
	v_pk_fma_f32 v[108:109], v[108:109], v[210:211], v[12:13]
	v_pk_fma_f32 v[98:99], v[98:99], v[210:211], v[2:3]
	v_pk_fma_f32 v[100:101], v[100:101], v[210:211], v[4:5]
	v_min_f32_e32 v106, 0x40e00000, v106
	v_min_f32_e32 v107, 0x40e00000, v107
	v_min_f32_e32 v108, 0x40e00000, v108
	v_min_f32_e32 v109, 0x40e00000, v109
	v_min_f32_e32 v98, 0x40e00000, v98
	v_min_f32_e32 v99, 0x40e00000, v99
	v_min_f32_e32 v100, 0x40e00000, v100
	v_min_f32_e32 v101, 0x40e00000, v101
	v_pk_mul_f32 v[202:203], v[106:107], v[212:213]
	v_pk_mul_f32 v[204:205], v[108:109], v[212:213]
	v_pk_mul_f32 v[206:207], v[98:99], v[212:213]
	v_pk_mul_f32 v[208:209], v[100:101], v[212:213]
	v_pk_fma_f32 v[110:111], v[110:111], v[210:211], v[14:15]
	v_pk_fma_f32 v[112:113], v[112:113], v[210:211], v[16:17]
	v_pk_fma_f32 v[102:103], v[102:103], v[210:211], v[6:7]
	v_pk_fma_f32 v[104:105], v[104:105], v[210:211], v[8:9]
	v_pk_mul_f32 v[202:203], v[202:203], v[214:215]
	v_pk_mul_f32 v[204:205], v[204:205], v[214:215]
	v_pk_mul_f32 v[206:207], v[206:207], v[214:215]
	v_pk_mul_f32 v[208:209], v[208:209], v[214:215]
	v_med3_f32 v110, v110, s37, v243
	v_med3_f32 v111, v111, s37, v243
	v_med3_f32 v112, v112, s37, v243
	v_med3_f32 v113, v113, s37, v243
	v_med3_f32 v102, v102, s37, v243
	v_med3_f32 v103, v103, s37, v243
	v_med3_f32 v104, v104, s37, v243
	v_med3_f32 v105, v105, s37, v243
	v_exp_f32_e32 v202, v202
	v_exp_f32_e32 v203, v203
	v_exp_f32_e32 v204, v204
	v_exp_f32_e32 v205, v205
	v_exp_f32_e32 v206, v206
	v_exp_f32_e32 v207, v207
	v_exp_f32_e32 v208, v208
	v_exp_f32_e32 v209, v209
	v_pk_add_f32 v[110:111], v[110:111], v[216:217]
	v_pk_add_f32 v[112:113], v[112:113], v[216:217]
	v_pk_add_f32 v[102:103], v[102:103], v[216:217]
	v_pk_add_f32 v[104:105], v[104:105], v[216:217]
	v_add_co_u32_e32 v194, vcc, 0xc000, v18
	v_pk_add_f32 v[202:203], v[202:203], v[216:217]
	v_pk_add_f32 v[204:205], v[204:205], v[216:217]
	v_pk_add_f32 v[206:207], v[206:207], v[216:217]
	v_pk_add_f32 v[208:209], v[208:209], v[216:217]
	v_addc_co_u32_e32 v195, vcc, 0, v19, vcc
	v_rcp_f32_e32 v202, v202
	v_rcp_f32_e32 v203, v203
	v_rcp_f32_e32 v204, v204
	v_rcp_f32_e32 v205, v205
	v_rcp_f32_e32 v206, v206
	v_rcp_f32_e32 v207, v207
	v_rcp_f32_e32 v208, v208
	v_rcp_f32_e32 v209, v209
	v_pk_mul_f32 v[106:107], v[106:107], v[202:203]
	v_pk_mul_f32 v[108:109], v[108:109], v[204:205]
	v_pk_mul_f32 v[98:99], v[98:99], v[206:207]
	v_pk_mul_f32 v[100:101], v[100:101], v[208:209]
	v_pk_mul_f32 v[106:107], v[110:111], v[106:107]
	v_pk_mul_f32 v[108:109], v[112:113], v[108:109]
	v_pk_mul_f32 v[98:99], v[102:103], v[98:99]
	v_pk_mul_f32 v[100:101], v[104:105], v[100:101]
	v_cvt_pk_fp8_f32 v196, v106, v107
	v_cvt_pk_fp8_f32 v197, v98, v99
	v_cvt_pk_fp8_f32 v196, v108, v109 op_sel:[0,0,1]
	v_cvt_pk_fp8_f32 v197, v100, v101 op_sel:[0,0,1]
	global_store_dwordx2 v[194:195], v[196:197], off
	v_pk_fma_f32 v[90:91], v[90:91], v[210:211], v[10:11]
	v_pk_fma_f32 v[92:93], v[92:93], v[210:211], v[12:13]
	v_pk_fma_f32 v[82:83], v[82:83], v[210:211], v[2:3]
	v_pk_fma_f32 v[84:85], v[84:85], v[210:211], v[4:5]
	v_min_f32_e32 v90, 0x40e00000, v90
	v_min_f32_e32 v91, 0x40e00000, v91
	v_min_f32_e32 v92, 0x40e00000, v92
	v_min_f32_e32 v93, 0x40e00000, v93
	v_min_f32_e32 v82, 0x40e00000, v82
	v_min_f32_e32 v83, 0x40e00000, v83
	v_min_f32_e32 v84, 0x40e00000, v84
	v_min_f32_e32 v85, 0x40e00000, v85
	v_pk_mul_f32 v[202:203], v[90:91], v[212:213]
	v_pk_mul_f32 v[204:205], v[92:93], v[212:213]
	v_pk_mul_f32 v[206:207], v[82:83], v[212:213]
	v_pk_mul_f32 v[208:209], v[84:85], v[212:213]
	v_pk_fma_f32 v[94:95], v[94:95], v[210:211], v[14:15]
	v_pk_fma_f32 v[96:97], v[96:97], v[210:211], v[16:17]
	v_pk_fma_f32 v[86:87], v[86:87], v[210:211], v[6:7]
	v_pk_fma_f32 v[88:89], v[88:89], v[210:211], v[8:9]
	v_pk_mul_f32 v[202:203], v[202:203], v[214:215]
	v_pk_mul_f32 v[204:205], v[204:205], v[214:215]
	v_pk_mul_f32 v[206:207], v[206:207], v[214:215]
	v_pk_mul_f32 v[208:209], v[208:209], v[214:215]
	v_med3_f32 v94, v94, s37, v243
	v_med3_f32 v95, v95, s37, v243
	v_med3_f32 v96, v96, s37, v243
	v_med3_f32 v97, v97, s37, v243
	v_med3_f32 v86, v86, s37, v243
	v_med3_f32 v87, v87, s37, v243
	v_med3_f32 v88, v88, s37, v243
	v_med3_f32 v89, v89, s37, v243
	v_exp_f32_e32 v202, v202
	v_exp_f32_e32 v203, v203
	v_exp_f32_e32 v204, v204
	v_exp_f32_e32 v205, v205
	v_exp_f32_e32 v206, v206
	v_exp_f32_e32 v207, v207
	v_exp_f32_e32 v208, v208
	v_exp_f32_e32 v209, v209
	v_pk_add_f32 v[94:95], v[94:95], v[216:217]
	v_pk_add_f32 v[96:97], v[96:97], v[216:217]
	v_pk_add_f32 v[86:87], v[86:87], v[216:217]
	v_pk_add_f32 v[88:89], v[88:89], v[216:217]
	v_add_co_u32_e32 v198, vcc, 0x20000, v18
	v_pk_add_f32 v[202:203], v[202:203], v[216:217]
	v_pk_add_f32 v[204:205], v[204:205], v[216:217]
	v_pk_add_f32 v[206:207], v[206:207], v[216:217]
	v_pk_add_f32 v[208:209], v[208:209], v[216:217]
	v_addc_co_u32_e32 v199, vcc, 0, v19, vcc
	v_rcp_f32_e32 v202, v202
	v_rcp_f32_e32 v203, v203
	v_rcp_f32_e32 v204, v204
	v_rcp_f32_e32 v205, v205
	v_rcp_f32_e32 v206, v206
	v_rcp_f32_e32 v207, v207
	v_rcp_f32_e32 v208, v208
	v_rcp_f32_e32 v209, v209
	v_pk_mul_f32 v[90:91], v[90:91], v[202:203]
	v_pk_mul_f32 v[92:93], v[92:93], v[204:205]
	v_pk_mul_f32 v[82:83], v[82:83], v[206:207]
	v_pk_mul_f32 v[84:85], v[84:85], v[208:209]
	v_pk_mul_f32 v[90:91], v[94:95], v[90:91]
	v_pk_mul_f32 v[92:93], v[96:97], v[92:93]
	v_pk_mul_f32 v[82:83], v[86:87], v[82:83]
	v_pk_mul_f32 v[84:85], v[88:89], v[84:85]
	v_cvt_pk_fp8_f32 v200, v90, v91
	v_cvt_pk_fp8_f32 v201, v82, v83
	v_cvt_pk_fp8_f32 v200, v92, v93 op_sel:[0,0,1]
	v_cvt_pk_fp8_f32 v201, v84, v85 op_sel:[0,0,1]
	global_store_dwordx2 v[198:199], v[200:201], off
	v_pk_fma_f32 v[74:75], v[74:75], v[210:211], v[10:11]
	v_pk_fma_f32 v[76:77], v[76:77], v[210:211], v[12:13]
	v_pk_fma_f32 v[66:67], v[66:67], v[210:211], v[2:3]
	v_pk_fma_f32 v[68:69], v[68:69], v[210:211], v[4:5]
	v_min_f32_e32 v74, 0x40e00000, v74
	v_min_f32_e32 v75, 0x40e00000, v75
	v_min_f32_e32 v76, 0x40e00000, v76
	v_min_f32_e32 v77, 0x40e00000, v77
	v_min_f32_e32 v66, 0x40e00000, v66
	v_min_f32_e32 v67, 0x40e00000, v67
	v_min_f32_e32 v68, 0x40e00000, v68
	v_min_f32_e32 v69, 0x40e00000, v69
	v_pk_mul_f32 v[202:203], v[74:75], v[212:213]
	v_pk_mul_f32 v[204:205], v[76:77], v[212:213]
	v_pk_mul_f32 v[206:207], v[66:67], v[212:213]
	v_pk_mul_f32 v[208:209], v[68:69], v[212:213]
	v_pk_fma_f32 v[78:79], v[78:79], v[210:211], v[14:15]
	v_pk_fma_f32 v[80:81], v[80:81], v[210:211], v[16:17]
	v_pk_fma_f32 v[70:71], v[70:71], v[210:211], v[6:7]
	v_pk_fma_f32 v[72:73], v[72:73], v[210:211], v[8:9]
	v_pk_mul_f32 v[202:203], v[202:203], v[214:215]
	v_pk_mul_f32 v[204:205], v[204:205], v[214:215]
	v_pk_mul_f32 v[206:207], v[206:207], v[214:215]
	v_pk_mul_f32 v[208:209], v[208:209], v[214:215]
	v_med3_f32 v78, v78, s37, v243
	v_med3_f32 v79, v79, s37, v243
	v_med3_f32 v80, v80, s37, v243
	v_med3_f32 v81, v81, s37, v243
	v_med3_f32 v70, v70, s37, v243
	v_med3_f32 v71, v71, s37, v243
	v_med3_f32 v72, v72, s37, v243
	v_med3_f32 v73, v73, s37, v243
	v_exp_f32_e32 v202, v202
	v_exp_f32_e32 v203, v203
	v_exp_f32_e32 v204, v204
	v_exp_f32_e32 v205, v205
	v_exp_f32_e32 v206, v206
	v_exp_f32_e32 v207, v207
	v_exp_f32_e32 v208, v208
	v_exp_f32_e32 v209, v209
	v_pk_add_f32 v[78:79], v[78:79], v[216:217]
	v_pk_add_f32 v[80:81], v[80:81], v[216:217]
	v_pk_add_f32 v[70:71], v[70:71], v[216:217]
	v_pk_add_f32 v[72:73], v[72:73], v[216:217]
	v_add_co_u32_e32 v194, vcc, 0x24000, v18
	v_pk_add_f32 v[202:203], v[202:203], v[216:217]
	v_pk_add_f32 v[204:205], v[204:205], v[216:217]
	v_pk_add_f32 v[206:207], v[206:207], v[216:217]
	v_pk_add_f32 v[208:209], v[208:209], v[216:217]
	v_addc_co_u32_e32 v195, vcc, 0, v19, vcc
	v_rcp_f32_e32 v202, v202
	v_rcp_f32_e32 v203, v203
	v_rcp_f32_e32 v204, v204
	v_rcp_f32_e32 v205, v205
	v_rcp_f32_e32 v206, v206
	v_rcp_f32_e32 v207, v207
	v_rcp_f32_e32 v208, v208
	v_rcp_f32_e32 v209, v209
	v_pk_mul_f32 v[74:75], v[74:75], v[202:203]
	v_pk_mul_f32 v[76:77], v[76:77], v[204:205]
	v_pk_mul_f32 v[66:67], v[66:67], v[206:207]
	v_pk_mul_f32 v[68:69], v[68:69], v[208:209]
	v_pk_mul_f32 v[74:75], v[78:79], v[74:75]
	v_pk_mul_f32 v[76:77], v[80:81], v[76:77]
	v_pk_mul_f32 v[66:67], v[70:71], v[66:67]
	v_pk_mul_f32 v[68:69], v[72:73], v[68:69]
	v_cvt_pk_fp8_f32 v196, v74, v75
	v_cvt_pk_fp8_f32 v197, v66, v67
	v_cvt_pk_fp8_f32 v196, v76, v77 op_sel:[0,0,1]
	v_cvt_pk_fp8_f32 v197, v68, v69 op_sel:[0,0,1]
	global_store_dwordx2 v[194:195], v[196:197], off
	v_pk_fma_f32 v[58:59], v[58:59], v[210:211], v[10:11]
	v_pk_fma_f32 v[60:61], v[60:61], v[210:211], v[12:13]
	v_pk_fma_f32 v[50:51], v[50:51], v[210:211], v[2:3]
	v_pk_fma_f32 v[52:53], v[52:53], v[210:211], v[4:5]
	v_min_f32_e32 v58, 0x40e00000, v58
	v_min_f32_e32 v59, 0x40e00000, v59
	v_min_f32_e32 v60, 0x40e00000, v60
	v_min_f32_e32 v61, 0x40e00000, v61
	v_min_f32_e32 v50, 0x40e00000, v50
	v_min_f32_e32 v51, 0x40e00000, v51
	v_min_f32_e32 v52, 0x40e00000, v52
	v_min_f32_e32 v53, 0x40e00000, v53
	v_pk_mul_f32 v[202:203], v[58:59], v[212:213]
	v_pk_mul_f32 v[204:205], v[60:61], v[212:213]
	v_pk_mul_f32 v[206:207], v[50:51], v[212:213]
	v_pk_mul_f32 v[208:209], v[52:53], v[212:213]
	v_pk_fma_f32 v[62:63], v[62:63], v[210:211], v[14:15]
	v_pk_fma_f32 v[64:65], v[64:65], v[210:211], v[16:17]
	v_pk_fma_f32 v[54:55], v[54:55], v[210:211], v[6:7]
	v_pk_fma_f32 v[56:57], v[56:57], v[210:211], v[8:9]
	v_pk_mul_f32 v[202:203], v[202:203], v[214:215]
	v_pk_mul_f32 v[204:205], v[204:205], v[214:215]
	v_pk_mul_f32 v[206:207], v[206:207], v[214:215]
	v_pk_mul_f32 v[208:209], v[208:209], v[214:215]
	v_med3_f32 v62, v62, s37, v243
	v_med3_f32 v63, v63, s37, v243
	v_med3_f32 v64, v64, s37, v243
	v_med3_f32 v65, v65, s37, v243
	v_med3_f32 v54, v54, s37, v243
	v_med3_f32 v55, v55, s37, v243
	v_med3_f32 v56, v56, s37, v243
	v_med3_f32 v57, v57, s37, v243
	v_exp_f32_e32 v202, v202
	v_exp_f32_e32 v203, v203
	v_exp_f32_e32 v204, v204
	v_exp_f32_e32 v205, v205
	v_exp_f32_e32 v206, v206
	v_exp_f32_e32 v207, v207
	v_exp_f32_e32 v208, v208
	v_exp_f32_e32 v209, v209
	v_pk_add_f32 v[62:63], v[62:63], v[216:217]
	v_pk_add_f32 v[64:65], v[64:65], v[216:217]
	v_pk_add_f32 v[54:55], v[54:55], v[216:217]
	v_pk_add_f32 v[56:57], v[56:57], v[216:217]
	v_add_co_u32_e32 v198, vcc, 0x28000, v18
	v_pk_add_f32 v[202:203], v[202:203], v[216:217]
	v_pk_add_f32 v[204:205], v[204:205], v[216:217]
	v_pk_add_f32 v[206:207], v[206:207], v[216:217]
	v_pk_add_f32 v[208:209], v[208:209], v[216:217]
	v_addc_co_u32_e32 v199, vcc, 0, v19, vcc
	v_rcp_f32_e32 v202, v202
	v_rcp_f32_e32 v203, v203
	v_rcp_f32_e32 v204, v204
	v_rcp_f32_e32 v205, v205
	v_rcp_f32_e32 v206, v206
	v_rcp_f32_e32 v207, v207
	v_rcp_f32_e32 v208, v208
	v_rcp_f32_e32 v209, v209
	v_pk_mul_f32 v[58:59], v[58:59], v[202:203]
	v_pk_mul_f32 v[60:61], v[60:61], v[204:205]
	v_pk_mul_f32 v[50:51], v[50:51], v[206:207]
	v_pk_mul_f32 v[52:53], v[52:53], v[208:209]
	v_pk_mul_f32 v[58:59], v[62:63], v[58:59]
	v_pk_mul_f32 v[60:61], v[64:65], v[60:61]
	v_pk_mul_f32 v[50:51], v[54:55], v[50:51]
	v_pk_mul_f32 v[52:53], v[56:57], v[52:53]
	v_cvt_pk_fp8_f32 v200, v58, v59
	v_cvt_pk_fp8_f32 v201, v50, v51
	v_cvt_pk_fp8_f32 v200, v60, v61 op_sel:[0,0,1]
	v_cvt_pk_fp8_f32 v201, v52, v53 op_sel:[0,0,1]
	global_store_dwordx2 v[198:199], v[200:201], off
	v_pk_fma_f32 v[42:43], v[42:43], v[210:211], v[10:11]
	v_pk_fma_f32 v[44:45], v[44:45], v[210:211], v[12:13]
	v_pk_fma_f32 v[38:39], v[38:39], v[210:211], v[2:3]
	v_pk_fma_f32 v[40:41], v[40:41], v[210:211], v[4:5]
	v_min_f32_e32 v42, 0x40e00000, v42
	v_min_f32_e32 v43, 0x40e00000, v43
	v_min_f32_e32 v44, 0x40e00000, v44
	v_min_f32_e32 v45, 0x40e00000, v45
	v_min_f32_e32 v38, 0x40e00000, v38
	v_min_f32_e32 v39, 0x40e00000, v39
	v_min_f32_e32 v40, 0x40e00000, v40
	v_min_f32_e32 v41, 0x40e00000, v41
	v_pk_mul_f32 v[202:203], v[42:43], v[212:213]
	v_pk_mul_f32 v[204:205], v[44:45], v[212:213]
	v_pk_mul_f32 v[206:207], v[38:39], v[212:213]
	v_pk_mul_f32 v[208:209], v[40:41], v[212:213]
	v_pk_fma_f32 v[46:47], v[46:47], v[210:211], v[14:15]
	v_pk_fma_f32 v[48:49], v[48:49], v[210:211], v[16:17]
	v_pk_fma_f32 v[34:35], v[34:35], v[210:211], v[6:7]
	v_pk_fma_f32 v[36:37], v[36:37], v[210:211], v[8:9]
	v_pk_mul_f32 v[202:203], v[202:203], v[214:215]
	v_pk_mul_f32 v[204:205], v[204:205], v[214:215]
	v_pk_mul_f32 v[206:207], v[206:207], v[214:215]
	v_pk_mul_f32 v[208:209], v[208:209], v[214:215]
	v_med3_f32 v46, v46, s37, v243
	v_med3_f32 v47, v47, s37, v243
	v_med3_f32 v48, v48, s37, v243
	v_med3_f32 v49, v49, s37, v243
	v_med3_f32 v34, v34, s37, v243
	v_med3_f32 v35, v35, s37, v243
	v_med3_f32 v36, v36, s37, v243
	v_med3_f32 v37, v37, s37, v243
	v_exp_f32_e32 v202, v202
	v_exp_f32_e32 v203, v203
	v_exp_f32_e32 v204, v204
	v_exp_f32_e32 v205, v205
	v_exp_f32_e32 v206, v206
	v_exp_f32_e32 v207, v207
	v_exp_f32_e32 v208, v208
	v_exp_f32_e32 v209, v209
	v_pk_add_f32 v[46:47], v[46:47], v[216:217]
	v_pk_add_f32 v[48:49], v[48:49], v[216:217]
	v_pk_add_f32 v[34:35], v[34:35], v[216:217]
	v_pk_add_f32 v[36:37], v[36:37], v[216:217]
	v_add_co_u32_e32 v194, vcc, 0x2c000, v18
	v_pk_add_f32 v[202:203], v[202:203], v[216:217]
	v_pk_add_f32 v[204:205], v[204:205], v[216:217]
	v_pk_add_f32 v[206:207], v[206:207], v[216:217]
	v_pk_add_f32 v[208:209], v[208:209], v[216:217]
	v_addc_co_u32_e32 v195, vcc, 0, v19, vcc
	v_rcp_f32_e32 v202, v202
	v_rcp_f32_e32 v203, v203
	v_rcp_f32_e32 v204, v204
	v_rcp_f32_e32 v205, v205
	v_rcp_f32_e32 v206, v206
	v_rcp_f32_e32 v207, v207
	v_rcp_f32_e32 v208, v208
	v_rcp_f32_e32 v209, v209
	v_pk_mul_f32 v[42:43], v[42:43], v[202:203]
	v_pk_mul_f32 v[44:45], v[44:45], v[204:205]
	v_pk_mul_f32 v[38:39], v[38:39], v[206:207]
	v_pk_mul_f32 v[40:41], v[40:41], v[208:209]
	v_pk_mul_f32 v[42:43], v[46:47], v[42:43]
	v_pk_mul_f32 v[44:45], v[48:49], v[44:45]
	v_pk_mul_f32 v[38:39], v[34:35], v[38:39]
	v_pk_mul_f32 v[40:41], v[36:37], v[40:41]
	v_cvt_pk_fp8_f32 v196, v42, v43
	v_cvt_pk_fp8_f32 v197, v38, v39
	v_cvt_pk_fp8_f32 v196, v44, v45 op_sel:[0,0,1]
	v_cvt_pk_fp8_f32 v197, v40, v41 op_sel:[0,0,1]
	global_store_dwordx2 v[194:195], v[196:197], off
	s_mov_b64 s[4:5], -1
	s_andn2_b64 vcc, exec, s[2:3]
	s_cbranch_vccnz .LBB0_1256
	s_andn2_b64 vcc, exec, s[10:11]
	s_cbranch_vccnz .LBB0_1255
	s_barrier
	s_branch .LBB0_1255
